# GEMM1 and GEMM2 K-loops: per-segment s_setprio flips removed, waves 4-7 at static priority 1
# baseline (speedup 1.0000x reference)
; #define LAS __attribute__((address_space(3)))
; #define IN(k) (fresh_tid(C), lo <= (k) && (k) < hi)
; __device__ __forceinline__ void moe_tables(const Ctx& C, LAS int* tb) {
;     if (C.tid < 64) { const unsigned* gcount = (const unsigned*)WSP(unsigned, WS_CTL) + CW_GCOUNT; const int e = C.tid & 31;
;         const int c = (int)__hip_atomic_load(gcount + e, __ATOMIC_RELAXED, __HIP_MEMORY_SCOPE_AGENT); const int tiles = (c + 255) >> 8; int incl = tiles;
; #pragma unroll
;         for (int o = 1; o < 32; o <<= 1) { const int v = __shfl_up(incl, o, 32); if (e >= o) incl += v; }
;         if (C.tid < 32) { tb[e] = incl - tiles; tb[33 + e] = c; if (e == 31) tb[32] = incl; } }
;     __syncthreads();
; }
; __global__ void __launch_bounds__(512, 2) mk_fwd(Args args) {
;     ...
;     if (IN(8)) for (int rep_ = 0; rep_ < 1 + ((MK_REPEAT >> 8) & 1); ++rep_) { if (rep_) xcd_barrier(bar); moe_tables(C, tb); pg8::Gemm g{WSP(bf16_t, WS_H), WSP(bf16_t, WS_W1T), 0, 4096, D_ / 2};   pg8::MoeOrder S; S.init_moe(16, C.G, C.bid, tb, C.ws, (LAS int*)(C.lds + LDS_MISC + 2048));
.LBB0_958:
	s_cmp_lt_i32 s82, 9
	s_cselect_b64 s[0:1], -1, 0
	s_cmp_gt_i32 s83, 8
	s_cselect_b64 s[2:3], -1, 0
	s_and_b64 s[0:1], s[0:1], s[2:3]
	v_mov_b32_e32 v1, v0
	v_cndmask_b32_e64 v2, 0, 1, s[0:1]
	v_cmp_ne_u32_e64 s[4:5], 1, v2
	s_andn2_b64 vcc, exec, s[0:1]
	s_mov_b64 s[76:77], s[24:25]
	s_cbranch_vccnz .LBB0_997
	v_readlane_b32 s0, v254, 4
	s_nop 0
	s_cmpk_lt_u32 s0, 0x100
	s_cbranch_scc1 .Lp8_prio_lo
	s_setprio 1
.Lp8_prio_lo:
	v_cmp_gt_i32_e32 vcc, 64, v1
	s_and_saveexec_b64 s[0:1], vcc
	s_cbranch_execz .LBB0_963
	v_and_b32_e32 v2, 31, v1
	v_lshlrev_b32_e32 v4, 2, v2
	v_mov_b32_e32 v5, 0
	v_lshl_add_u64 v[4:5], s[62:63], 0, v[4:5]
	v_add_co_u32_e32 v4, vcc, 0x4000, v4
	s_nop 1
	v_addc_co_u32_e32 v5, vcc, 0, v5, vcc
	s_waitcnt lgkmcnt(0)
	global_load_dword v3, v[4:5], off sc1
	v_mbcnt_lo_u32_b32 v4, -1, 0
	v_mbcnt_hi_u32_b32 v5, -1, v4
	v_and_b32_e32 v6, 0x60, v5
	v_add_u32_e32 v4, -1, v5
	v_cmp_lt_i32_e32 vcc, v4, v6
	v_add_u32_e32 v7, -2, v5
	v_add_u32_e32 v8, -4, v5
	v_cndmask_b32_e32 v4, v4, v5, vcc
	v_lshlrev_b32_e32 v10, 2, v4
	v_cmp_lt_i32_e32 vcc, v7, v6
	v_add_u32_e32 v9, -8, v5
	s_waitcnt vmcnt(0)
	v_add_u32_e32 v4, 0xff, v3
	v_ashrrev_i32_e32 v4, 8, v4
	ds_bpermute_b32 v10, v10, v4
	v_cndmask_b32_e32 v7, v7, v5, vcc
	v_cmp_ne_u32_e32 vcc, 0, v2
	v_lshlrev_b32_e32 v7, 2, v7
	s_waitcnt lgkmcnt(0)
	v_cndmask_b32_e32 v10, 0, v10, vcc
	v_add_u32_e32 v10, v10, v4
	ds_bpermute_b32 v7, v7, v10
	v_cmp_lt_i32_e32 vcc, v8, v6
	s_nop 1
	v_cndmask_b32_e32 v8, v8, v5, vcc
	v_cmp_lt_u32_e32 vcc, 1, v2
	v_lshlrev_b32_e32 v8, 2, v8
	s_waitcnt lgkmcnt(0)
	v_cndmask_b32_e32 v7, 0, v7, vcc
	v_add_u32_e32 v7, v7, v10
	ds_bpermute_b32 v8, v8, v7
	v_cmp_lt_i32_e32 vcc, v9, v6
	s_nop 1
	v_cndmask_b32_e32 v9, v9, v5, vcc
	v_cmp_lt_u32_e32 vcc, 3, v2
	v_lshlrev_b32_e32 v9, 2, v9
	s_waitcnt lgkmcnt(0)
	v_cndmask_b32_e32 v8, 0, v8, vcc
	v_add_u32_e32 v7, v8, v7
	ds_bpermute_b32 v8, v9, v7
	v_add_u32_e32 v9, -16, v5
	v_cmp_lt_i32_e32 vcc, v9, v6
	s_nop 1
	v_cndmask_b32_e32 v6, v9, v5, vcc
	v_cmp_lt_u32_e32 vcc, 7, v2
	v_lshlrev_b32_e32 v6, 2, v6
	s_waitcnt lgkmcnt(0)
	v_cndmask_b32_e32 v5, 0, v8, vcc
	v_add_u32_e32 v5, v5, v7
	ds_bpermute_b32 v6, v6, v5
	v_cmp_gt_i32_e32 vcc, 32, v1
	s_and_b64 exec, exec, vcc
	s_cbranch_execz .LBB0_963
	v_cmp_lt_u32_e32 vcc, 15, v2
	s_waitcnt lgkmcnt(0)
	s_nop 0
	v_cndmask_b32_e32 v1, 0, v6, vcc
	v_add_u32_e32 v1, v1, v5
	v_lshl_add_u32 v5, v2, 2, 0
	v_add_u32_e32 v5, 0x22040, v5
	v_cmp_eq_u32_e32 vcc, 31, v2
	v_sub_u32_e32 v2, v1, v4
	ds_write2_b32 v5, v2, v3 offset1:33
	s_and_b64 exec, exec, vcc
	s_add_i32 s2, 0, 0x220c0
	v_mov_b32_e32 v2, s2
	ds_write_b32 v2, v1

.LBB0_990:
	s_lshl_b32 s0, s64, 19
	s_and_b64 s[22:23], s[34:35], exec
	s_cselect_b32 s1, s0, s68
	s_add_i32 s18, s18, 0
	s_add_i32 s18, s18, 0x20000
	v_mov_b32_e32 v34, 0
	v_add3_u32 v180, s18, v171, v172
	v_add3_u32 v181, s18, v173, v174
	s_mov_b32 s70, -2
	s_movk_i32 s71, 0x100
	ds_read_b128 v[2:5], v176
	ds_read_b128 v[6:9], v176 offset:1024
	ds_read_b128 v[10:13], v176 offset:2048
	ds_read_b128 v[14:17], v176 offset:3072
	s_add_i32 s72, s68, s71
	s_cmp_eq_u32 s70, 12
	s_cselect_b64 s[22:23], -1, 0
	s_and_b64 s[18:19], s[22:23], exec
	s_cselect_b32 s72, s1, s72
	s_add_i32 s18, s71, 0xffffff80
	s_mov_b32 m0, s51
	ds_read_b128 v[182:185], v177
	ds_read_b128 v[186:189], v177 offset:1024
	ds_read_b128 v[190:193], v177 offset:2048
	ds_read_b128 v[194:197], v177 offset:3072
	ds_read_b128 v[198:201], v177 offset:4096
	ds_read_b128 v[202:205], v177 offset:5120
	ds_read_b128 v[206:209], v177 offset:6144
	ds_read_b128 v[210:213], v177 offset:7168
	buffer_load_dwordx4 v165, s[12:15], s18 offen lds
	s_mov_b32 m0, s52
	s_nop 0
	buffer_load_dwordx4 v169, s[12:15], s18 offen lds
	s_waitcnt lgkmcnt(8)
	s_barrier
	s_waitcnt lgkmcnt(0)
	s_nop 0
	s_waitcnt lgkmcnt(6)
	v_mfma_f32_16x16x128_f8f6f4 v[142:145], v[2:9], v[182:189], 0
	v_mfma_f32_16x16x128_f8f6f4 v[134:137], v[10:17], v[182:189], 0
	s_waitcnt lgkmcnt(4)
	v_mfma_f32_16x16x128_f8f6f4 v[126:129], v[2:9], v[190:197], 0
	v_mfma_f32_16x16x128_f8f6f4 v[118:121], v[10:17], v[190:197], 0
	s_waitcnt lgkmcnt(2)
	v_mfma_f32_16x16x128_f8f6f4 v[146:149], v[2:9], v[198:205], 0
	v_mfma_f32_16x16x128_f8f6f4 v[150:153], v[10:17], v[198:205], 0
	s_waitcnt lgkmcnt(0)
	v_mfma_f32_16x16x128_f8f6f4 v[154:157], v[2:9], v[206:213], 0
	v_mfma_f32_16x16x128_f8f6f4 v[158:161], v[10:17], v[206:213], 0
	s_nop 0
	s_barrier
	s_mov_b32 s18, s14
	s_mov_b32 s19, s15
	s_mov_b32 m0, s33
	s_nop 1
	ds_read_b128 v[18:21], v178
	ds_read_b128 v[22:25], v178 offset:1024
	ds_read_b128 v[26:29], v178 offset:2048
	ds_read_b128 v[30:33], v178 offset:3072
	buffer_load_dwordx4 v166, s[16:19], s72 offen lds
	s_mov_b32 m0, s36
	s_nop 0
	buffer_load_dwordx4 v168, s[16:19], s72 offen lds
	s_barrier
	s_waitcnt lgkmcnt(0)
	s_nop 0
	s_waitcnt lgkmcnt(2)
	v_mfma_f32_16x16x128_f8f6f4 v[138:141], v[18:25], v[182:189], 0
	s_and_b64 s[74:75], s[34:35], s[22:23]
	s_waitcnt lgkmcnt(0)
	v_mfma_f32_16x16x128_f8f6f4 v[130:133], v[26:33], v[182:189], 0
	v_mfma_f32_16x16x128_f8f6f4 v[122:125], v[18:25], v[190:197], 0
	v_mfma_f32_16x16x128_f8f6f4 v[114:117], v[26:33], v[190:197], 0
	v_mfma_f32_16x16x128_f8f6f4 v[110:113], v[18:25], v[198:205], 0
	v_mfma_f32_16x16x128_f8f6f4 v[106:109], v[26:33], v[198:205], 0
	v_mfma_f32_16x16x128_f8f6f4 v[102:105], v[18:25], v[206:213], 0
	v_mfma_f32_16x16x128_f8f6f4 v[98:101], v[26:33], v[206:213], 0
	s_nop 0
	s_andn2_b64 vcc, exec, s[74:75]
	s_barrier
	s_or_b32 s73, s72, 0x80
	s_and_b64 s[22:23], s[22:23], exec
	s_mov_b32 m0, s29
	s_cselect_b32 s22, 0, s71
	ds_read_b128 v[182:185], v177 offset:16384
	ds_read_b128 v[186:189], v177 offset:17408
	ds_read_b128 v[190:193], v177 offset:18432
	ds_read_b128 v[194:197], v177 offset:19456
	ds_read_b128 v[198:201], v177 offset:20480
	ds_read_b128 v[202:205], v177 offset:21504
	ds_read_b128 v[206:209], v177 offset:22528
	ds_read_b128 v[210:213], v177 offset:23552
	buffer_load_dwordx4 v164, s[12:15], s22 offen lds
	s_mov_b32 m0, s37
	s_or_b32 s23, s22, 0x80
	buffer_load_dwordx4 v167, s[12:15], s22 offen lds
	s_barrier
	s_waitcnt lgkmcnt(0)
	s_nop 0
	s_waitcnt lgkmcnt(6)
	v_mfma_f32_16x16x128_f8f6f4 v[94:97], v[2:9], v[182:189], 0
	v_mfma_f32_16x16x128_f8f6f4 v[86:89], v[10:17], v[182:189], 0
	s_waitcnt lgkmcnt(4)
	v_mfma_f32_16x16x128_f8f6f4 v[78:81], v[2:9], v[190:197], 0
	v_mfma_f32_16x16x128_f8f6f4 v[70:73], v[10:17], v[190:197], 0
	s_waitcnt lgkmcnt(2)
	v_mfma_f32_16x16x128_f8f6f4 v[214:217], v[2:9], v[198:205], 0
	v_mfma_f32_16x16x128_f8f6f4 v[218:221], v[10:17], v[198:205], 0
	s_waitcnt lgkmcnt(0)
	v_mfma_f32_16x16x128_f8f6f4 v[222:225], v[2:9], v[206:213], 0
	v_mfma_f32_16x16x128_f8f6f4 v[226:229], v[10:17], v[206:213], 0
	s_nop 0
	s_barrier
	s_add_i32 s74, s72, 0x40000
	s_mov_b32 m0, s38
	s_nop 0
	buffer_load_dwordx4 v166, s[16:19], s74 offen lds
	s_mov_b32 m0, s39
	s_nop 0
	buffer_load_dwordx4 v168, s[16:19], s74 offen lds
	s_waitcnt vmcnt(6)
	s_barrier
	s_nop 0
	v_mfma_f32_16x16x128_f8f6f4 v[90:93], v[18:25], v[182:189], 0
	v_mfma_f32_16x16x128_f8f6f4 v[82:85], v[26:33], v[182:189], 0
	v_mfma_f32_16x16x128_f8f6f4 v[74:77], v[18:25], v[190:197], 0
	v_mfma_f32_16x16x128_f8f6f4 v[66:69], v[26:33], v[190:197], 0
	v_mfma_f32_16x16x128_f8f6f4 v[230:233], v[18:25], v[198:205], 0
	v_mfma_f32_16x16x128_f8f6f4 v[234:237], v[26:33], v[198:205], 0
	v_mfma_f32_16x16x128_f8f6f4 v[238:241], v[18:25], v[206:213], 0
	v_mfma_f32_16x16x128_f8f6f4 v[242:245], v[26:33], v[206:213], 0
	s_nop 0
	v_add_u32_e32 v14, 0x18000, v175
	s_barrier
	s_branch .Lmid_g1
.LBB0_991:
	s_or_b32 s73, s72, 0x80
	s_and_b64 s[22:23], s[22:23], exec
	s_mov_b32 m0, s29
	s_cselect_b32 s22, 0, s71
	ds_read_b128 v[182:185], v177 offset:16384
	ds_read_b128 v[186:189], v177 offset:17408
	ds_read_b128 v[190:193], v177 offset:18432
	ds_read_b128 v[194:197], v177 offset:19456
	ds_read_b128 v[198:201], v177 offset:20480
	ds_read_b128 v[202:205], v177 offset:21504
	ds_read_b128 v[206:209], v177 offset:22528
	ds_read_b128 v[210:213], v177 offset:23552
	buffer_load_dwordx4 v164, s[12:15], s22 offen lds
	s_mov_b32 m0, s37
	s_or_b32 s23, s22, 0x80
	buffer_load_dwordx4 v167, s[12:15], s22 offen lds
	s_barrier
	s_waitcnt lgkmcnt(0)
	s_nop 0
	s_waitcnt lgkmcnt(6)
	v_mfma_f32_16x16x128_f8f6f4 v[94:97], v[2:9], v[182:189], v[94:97]
	v_mfma_f32_16x16x128_f8f6f4 v[86:89], v[10:17], v[182:189], v[86:89]
	s_waitcnt lgkmcnt(4)
	v_mfma_f32_16x16x128_f8f6f4 v[78:81], v[2:9], v[190:197], v[78:81]
	v_mfma_f32_16x16x128_f8f6f4 v[70:73], v[10:17], v[190:197], v[70:73]
	s_waitcnt lgkmcnt(2)
	v_mfma_f32_16x16x128_f8f6f4 v[214:217], v[2:9], v[198:205], v[62:65]
	v_mfma_f32_16x16x128_f8f6f4 v[218:221], v[10:17], v[198:205], v[54:57]
	s_waitcnt lgkmcnt(0)
	v_mfma_f32_16x16x128_f8f6f4 v[222:225], v[2:9], v[206:213], v[46:49]
	v_mfma_f32_16x16x128_f8f6f4 v[226:229], v[10:17], v[206:213], v[38:41]
	s_nop 0
	s_barrier
	s_add_i32 s74, s72, 0x40000
	s_mov_b32 m0, s38
	s_nop 0
	buffer_load_dwordx4 v166, s[16:19], s74 offen lds
	s_mov_b32 m0, s39
	s_nop 0
	buffer_load_dwordx4 v168, s[16:19], s74 offen lds
	s_waitcnt vmcnt(6)
	s_barrier
	s_nop 0
	v_mfma_f32_16x16x128_f8f6f4 v[90:93], v[18:25], v[182:189], v[90:93]
	v_mfma_f32_16x16x128_f8f6f4 v[82:85], v[26:33], v[182:189], v[82:85]
	v_mfma_f32_16x16x128_f8f6f4 v[74:77], v[18:25], v[190:197], v[74:77]
	v_mfma_f32_16x16x128_f8f6f4 v[66:69], v[26:33], v[190:197], v[66:69]
	v_mfma_f32_16x16x128_f8f6f4 v[230:233], v[18:25], v[198:205], v[58:61]
	v_mfma_f32_16x16x128_f8f6f4 v[234:237], v[26:33], v[198:205], v[50:53]
	v_mfma_f32_16x16x128_f8f6f4 v[238:241], v[18:25], v[206:213], v[42:45]
	v_mfma_f32_16x16x128_f8f6f4 v[242:245], v[26:33], v[206:213], v[34:37]
	s_nop 0
	v_add_u32_e32 v14, 0x18000, v175
	s_barrier
.Lmid_g1:
	ds_read_b128 v[2:5], v14
	ds_read_b128 v[6:9], v14 offset:1024
	ds_read_b128 v[10:13], v14 offset:2048
	ds_read_b128 v[14:17], v14 offset:3072
	s_mov_b32 m0, s40
	ds_read_b128 v[34:37], v177 offset:32768
	ds_read_b128 v[38:41], v177 offset:33792
	ds_read_b128 v[42:45], v177 offset:34816
	ds_read_b128 v[46:49], v177 offset:35840
	ds_read_b128 v[50:53], v177 offset:36864
	ds_read_b128 v[54:57], v177 offset:37888
	ds_read_b128 v[58:61], v177 offset:38912
	ds_read_b128 v[62:65], v177 offset:39936
	buffer_load_dwordx4 v165, s[12:15], s22 offen lds
	s_mov_b32 m0, s41
	s_nop 0
	buffer_load_dwordx4 v169, s[12:15], s22 offen lds
	s_waitcnt lgkmcnt(8)
	s_barrier
	s_waitcnt lgkmcnt(0)
	s_nop 0
	s_waitcnt lgkmcnt(6)
	v_mfma_f32_16x16x128_f8f6f4 v[142:145], v[2:9], v[34:41], v[142:145]
	v_mfma_f32_16x16x128_f8f6f4 v[134:137], v[10:17], v[34:41], v[134:137]
	s_waitcnt lgkmcnt(4)
	v_mfma_f32_16x16x128_f8f6f4 v[126:129], v[2:9], v[42:49], v[126:129]
	v_mfma_f32_16x16x128_f8f6f4 v[118:121], v[10:17], v[42:49], v[118:121]
	s_waitcnt lgkmcnt(2)
	v_mfma_f32_16x16x128_f8f6f4 v[30:33], v[2:9], v[50:57], v[146:149]
	v_mfma_f32_16x16x128_f8f6f4 v[26:29], v[10:17], v[50:57], v[150:153]
	s_waitcnt lgkmcnt(0)
	v_mfma_f32_16x16x128_f8f6f4 v[22:25], v[2:9], v[58:65], v[154:157]
	v_mfma_f32_16x16x128_f8f6f4 v[18:21], v[10:17], v[58:65], v[158:161]
	s_nop 0
	s_barrier
	s_nop 4
	v_add_u32_e32 v158, 0x1c000, v175
	s_mov_b32 m0, s45
	ds_read_b128 v[146:149], v158
	ds_read_b128 v[150:153], v158 offset:1024
	ds_read_b128 v[154:157], v158 offset:2048
	ds_read_b128 v[158:161], v158 offset:3072
	buffer_load_dwordx4 v166, s[16:19], s73 offen lds
	s_mov_b32 m0, s46
	s_nop 0
	buffer_load_dwordx4 v168, s[16:19], s73 offen lds
	s_barrier
	s_waitcnt lgkmcnt(0)
	s_nop 0
	s_waitcnt lgkmcnt(2)
	v_mfma_f32_16x16x128_f8f6f4 v[138:141], v[146:153], v[34:41], v[138:141]
	s_waitcnt lgkmcnt(0)
	v_mfma_f32_16x16x128_f8f6f4 v[130:133], v[154:161], v[34:41], v[130:133]
	v_mfma_f32_16x16x128_f8f6f4 v[122:125], v[146:153], v[42:49], v[122:125]
	v_mfma_f32_16x16x128_f8f6f4 v[114:117], v[154:161], v[42:49], v[114:117]
	v_mfma_f32_16x16x128_f8f6f4 v[110:113], v[146:153], v[50:57], v[110:113]
	v_mfma_f32_16x16x128_f8f6f4 v[106:109], v[154:161], v[50:57], v[106:109]
	v_mfma_f32_16x16x128_f8f6f4 v[102:105], v[146:153], v[58:65], v[102:105]
	v_mfma_f32_16x16x128_f8f6f4 v[98:101], v[154:161], v[58:65], v[98:101]
	s_nop 0
	s_mov_b32 m0, s47
	s_barrier
	ds_read_b128 v[182:185], v177 offset:49152
	ds_read_b128 v[186:189], v177 offset:50176
	ds_read_b128 v[190:193], v177 offset:51200
	ds_read_b128 v[194:197], v177 offset:52224
	ds_read_b128 v[198:201], v177 offset:53248
	ds_read_b128 v[202:205], v177 offset:54272
	ds_read_b128 v[206:209], v177 offset:55296
	ds_read_b128 v[210:213], v177 offset:56320
	buffer_load_dwordx4 v164, s[12:15], s23 offen lds
	s_mov_b32 m0, s48
	s_nop 0
	buffer_load_dwordx4 v167, s[12:15], s23 offen lds
	s_barrier
	s_waitcnt lgkmcnt(0)
	s_nop 0
	s_waitcnt lgkmcnt(6)
	v_mfma_f32_16x16x128_f8f6f4 v[94:97], v[2:9], v[182:189], v[94:97]
	v_mfma_f32_16x16x128_f8f6f4 v[86:89], v[10:17], v[182:189], v[86:89]
	s_waitcnt lgkmcnt(4)
	v_mfma_f32_16x16x128_f8f6f4 v[78:81], v[2:9], v[190:197], v[78:81]
	v_mfma_f32_16x16x128_f8f6f4 v[70:73], v[10:17], v[190:197], v[70:73]
	s_waitcnt lgkmcnt(2)
	v_mfma_f32_16x16x128_f8f6f4 v[62:65], v[2:9], v[198:205], v[214:217]
	v_mfma_f32_16x16x128_f8f6f4 v[54:57], v[10:17], v[198:205], v[218:221]
	s_waitcnt lgkmcnt(0)
	v_mfma_f32_16x16x128_f8f6f4 v[46:49], v[2:9], v[206:213], v[222:225]
	v_mfma_f32_16x16x128_f8f6f4 v[38:41], v[10:17], v[206:213], v[226:229]
	s_nop 0
	s_barrier
	s_add_i32 s72, s72, 0x40080
	s_mov_b32 m0, s49
	s_nop 0
	buffer_load_dwordx4 v166, s[16:19], s72 offen lds
	s_mov_b32 m0, s50
	s_nop 0
	buffer_load_dwordx4 v168, s[16:19], s72 offen lds
	s_waitcnt vmcnt(6)
	s_barrier
	s_nop 0
	v_mfma_f32_16x16x128_f8f6f4 v[90:93], v[146:153], v[182:189], v[90:93]
	v_mfma_f32_16x16x128_f8f6f4 v[82:85], v[154:161], v[182:189], v[82:85]
	v_mfma_f32_16x16x128_f8f6f4 v[74:77], v[146:153], v[190:197], v[74:77]
	v_mfma_f32_16x16x128_f8f6f4 v[66:69], v[154:161], v[190:197], v[66:69]
	v_mfma_f32_16x16x128_f8f6f4 v[58:61], v[146:153], v[198:205], v[230:233]
	v_mfma_f32_16x16x128_f8f6f4 v[50:53], v[154:161], v[198:205], v[234:237]
	v_mfma_f32_16x16x128_f8f6f4 v[42:45], v[146:153], v[206:213], v[238:241]
	v_mfma_f32_16x16x128_f8f6f4 v[34:37], v[154:161], v[206:213], v[242:245]
	s_nop 0
	s_add_i32 s70, s70, 2
	s_addk_i32 s71, 0x100
	s_cmp_gt_u32 s70, 13
	s_barrier
	s_cbranch_scc1 .LBB0_979
.LBB0_992:
	ds_read_b128 v[2:5], v176
	ds_read_b128 v[6:9], v176 offset:1024
	ds_read_b128 v[10:13], v176 offset:2048
	ds_read_b128 v[14:17], v176 offset:3072
	s_add_i32 s72, s68, s71
	s_cmp_eq_u32 s70, 12
	s_cselect_b64 s[22:23], -1, 0
	s_and_b64 s[18:19], s[22:23], exec
	s_cselect_b32 s72, s1, s72
	s_add_i32 s18, s71, 0xffffff80
	s_mov_b32 m0, s51
	ds_read_b128 v[182:185], v177
	ds_read_b128 v[186:189], v177 offset:1024
	ds_read_b128 v[190:193], v177 offset:2048
	ds_read_b128 v[194:197], v177 offset:3072
	ds_read_b128 v[198:201], v177 offset:4096
	ds_read_b128 v[202:205], v177 offset:5120
	ds_read_b128 v[206:209], v177 offset:6144
	ds_read_b128 v[210:213], v177 offset:7168
	buffer_load_dwordx4 v165, s[12:15], s18 offen lds
	s_mov_b32 m0, s52
	s_nop 0
	buffer_load_dwordx4 v169, s[12:15], s18 offen lds
	s_waitcnt lgkmcnt(8)
	s_barrier
	s_waitcnt lgkmcnt(0)
	s_nop 0
	s_waitcnt lgkmcnt(6)
	v_mfma_f32_16x16x128_f8f6f4 v[142:145], v[2:9], v[182:189], v[142:145]
	v_mfma_f32_16x16x128_f8f6f4 v[134:137], v[10:17], v[182:189], v[134:137]
	s_waitcnt lgkmcnt(4)
	v_mfma_f32_16x16x128_f8f6f4 v[126:129], v[2:9], v[190:197], v[126:129]
	v_mfma_f32_16x16x128_f8f6f4 v[118:121], v[10:17], v[190:197], v[118:121]
	s_waitcnt lgkmcnt(2)
	v_mfma_f32_16x16x128_f8f6f4 v[146:149], v[2:9], v[198:205], v[30:33]
	v_mfma_f32_16x16x128_f8f6f4 v[150:153], v[10:17], v[198:205], v[26:29]
	s_waitcnt lgkmcnt(0)
	v_mfma_f32_16x16x128_f8f6f4 v[154:157], v[2:9], v[206:213], v[22:25]
	v_mfma_f32_16x16x128_f8f6f4 v[158:161], v[10:17], v[206:213], v[18:21]
	s_nop 0
	s_barrier
	s_mov_b32 s18, s14
	s_mov_b32 s19, s15
	s_mov_b32 m0, s33
	s_nop 1
	ds_read_b128 v[18:21], v178
	ds_read_b128 v[22:25], v178 offset:1024
	ds_read_b128 v[26:29], v178 offset:2048
	ds_read_b128 v[30:33], v178 offset:3072
	buffer_load_dwordx4 v166, s[16:19], s72 offen lds
	s_mov_b32 m0, s36
	s_nop 0
	buffer_load_dwordx4 v168, s[16:19], s72 offen lds
	s_barrier
	s_waitcnt lgkmcnt(0)
	s_nop 0
	s_waitcnt lgkmcnt(2)
	v_mfma_f32_16x16x128_f8f6f4 v[138:141], v[18:25], v[182:189], v[138:141]
	s_and_b64 s[74:75], s[34:35], s[22:23]
	s_waitcnt lgkmcnt(0)
	v_mfma_f32_16x16x128_f8f6f4 v[130:133], v[26:33], v[182:189], v[130:133]
	v_mfma_f32_16x16x128_f8f6f4 v[122:125], v[18:25], v[190:197], v[122:125]
	v_mfma_f32_16x16x128_f8f6f4 v[114:117], v[26:33], v[190:197], v[114:117]
	v_mfma_f32_16x16x128_f8f6f4 v[110:113], v[18:25], v[198:205], v[110:113]
	v_mfma_f32_16x16x128_f8f6f4 v[106:109], v[26:33], v[198:205], v[106:109]
	v_mfma_f32_16x16x128_f8f6f4 v[102:105], v[18:25], v[206:213], v[102:105]
	v_mfma_f32_16x16x128_f8f6f4 v[98:101], v[26:33], v[206:213], v[98:101]
	s_nop 0
	s_andn2_b64 vcc, exec, s[74:75]
	s_barrier
	s_cbranch_vccnz .LBB0_991
	ds_read2st64_b32 v[164:165], v180 offset1:2
	ds_read2st64_b32 v[182:183], v181 offset1:2
	s_waitcnt lgkmcnt(0)
	s_waitcnt lgkmcnt(1)
	v_lshlrev_b32_e32 v164, 9, v164
	v_lshlrev_b32_e32 v165, 9, v165
	s_waitcnt lgkmcnt(0)
	v_lshlrev_b32_e32 v167, 9, v182
	v_lshlrev_b32_e32 v169, 9, v183
	v_and_b32_e32 v164, 0xfffff800, v164
	v_and_b32_e32 v165, 0xfffff800, v165
	v_and_b32_e32 v167, 0xfffff800, v167
	v_and_b32_e32 v169, 0xfffff800, v169
	v_add_u32_e32 v164, v164, v162
	v_add_u32_e32 v165, v165, v162
	v_add_u32_e32 v167, v167, v163
	v_add_u32_e32 v169, v169, v163
	s_branch .LBB0_991

.LBB0_1080:
	s_lshl_b32 s10, s60, 19
	s_and_b64 s[18:19], s[0:1], exec
	s_cselect_b32 s18, s10, s67
	s_lshl_b32 s11, s62, 19
	s_and_b64 s[0:1], s[0:1], exec
	v_mov_b32_e32 v26, 0
	s_cselect_b32 s0, s11, s66
	s_add_i32 s1, s67, 0x40080
	s_add_i32 s19, s66, 0x100
	s_mov_b32 s66, -2
	s_waitcnt lgkmcnt(0)
	ds_read_b128 v[126:129], v153
	ds_read_b128 v[130:133], v153 offset:1024
	ds_read_b128 v[138:141], v153 offset:2048
	ds_read_b128 v[142:145], v153 offset:3072
	s_add_i32 s26, s1, 0xfffc0080
	s_cmp_eq_u32 s66, 12
	s_cselect_b32 s69, s18, s26
	s_cselect_b32 s67, s0, s19
	s_or_b32 s68, s69, 0x80
	s_mov_b32 m0, s51
	ds_read_b128 v[160:163], v154
	ds_read_b128 v[164:167], v154 offset:1024
	ds_read_b128 v[168:171], v154 offset:2048
	ds_read_b128 v[172:175], v154 offset:3072
	ds_read_b128 v[176:179], v154 offset:4096
	ds_read_b128 v[180:183], v154 offset:5120
	ds_read_b128 v[184:187], v154 offset:6144
	ds_read_b128 v[188:191], v154 offset:7168
	buffer_load_dwordx4 v1, s[20:23], s1 offen lds
	s_mov_b32 m0, s52
	s_nop 0
	buffer_load_dwordx4 v252, s[20:23], s1 offen lds
	s_waitcnt lgkmcnt(8)
	s_barrier
	s_waitcnt lgkmcnt(0)
	s_nop 0
	s_waitcnt lgkmcnt(6)
	v_mfma_f32_16x16x128_f8f6f4 v[134:137], v[126:133], v[160:167], 0
	v_mfma_f32_16x16x128_f8f6f4 v[122:125], v[138:145], v[160:167], 0
	s_waitcnt lgkmcnt(4)
	v_mfma_f32_16x16x128_f8f6f4 v[192:195], v[126:133], v[168:175], 0
	v_mfma_f32_16x16x128_f8f6f4 v[196:199], v[138:145], v[168:175], 0
	s_waitcnt lgkmcnt(2)
	v_mfma_f32_16x16x128_f8f6f4 v[200:203], v[126:133], v[176:183], 0
	v_mfma_f32_16x16x128_f8f6f4 v[204:207], v[138:145], v[176:183], 0
	s_waitcnt lgkmcnt(0)
	v_mfma_f32_16x16x128_f8f6f4 v[208:211], v[126:133], v[184:191], 0
	v_mfma_f32_16x16x128_f8f6f4 v[212:215], v[138:145], v[184:191], 0
	s_nop 0
	s_barrier
	s_mov_b32 s26, s22
	s_mov_b32 s27, s23
	s_mov_b32 m0, s36
	s_nop 1
	ds_read_b128 v[74:77], v155
	ds_read_b128 v[78:81], v155 offset:1024
	ds_read_b128 v[90:93], v155 offset:2048
	ds_read_b128 v[94:97], v155 offset:3072
	buffer_load_dwordx4 v253, s[24:27], s67 offen lds
	s_mov_b32 m0, s37
	s_nop 0
	buffer_load_dwordx4 v150, s[24:27], s67 offen lds
	s_barrier
	s_waitcnt lgkmcnt(0)
	s_nop 0
	s_waitcnt lgkmcnt(2)
	v_mfma_f32_16x16x128_f8f6f4 v[118:121], v[74:81], v[160:167], 0
	s_waitcnt lgkmcnt(0)
	v_mfma_f32_16x16x128_f8f6f4 v[114:117], v[90:97], v[160:167], 0
	v_mfma_f32_16x16x128_f8f6f4 v[160:163], v[74:81], v[168:175], 0
	v_mfma_f32_16x16x128_f8f6f4 v[164:167], v[90:97], v[168:175], 0
	v_mfma_f32_16x16x128_f8f6f4 v[168:171], v[74:81], v[176:183], 0
	v_mfma_f32_16x16x128_f8f6f4 v[172:175], v[90:97], v[176:183], 0
	v_mfma_f32_16x16x128_f8f6f4 v[176:179], v[74:81], v[184:191], 0
	v_mfma_f32_16x16x128_f8f6f4 v[180:183], v[90:97], v[184:191], 0
	s_nop 0
	s_mov_b32 m0, s35
	s_barrier
	s_nop 3
	ds_read_b128 v[66:69], v154 offset:16384
	ds_read_b128 v[70:73], v154 offset:17408
	ds_read_b128 v[82:85], v154 offset:18432
	ds_read_b128 v[86:89], v154 offset:19456
	ds_read_b128 v[98:101], v154 offset:20480
	ds_read_b128 v[102:105], v154 offset:21504
	ds_read_b128 v[106:109], v154 offset:22528
	ds_read_b128 v[110:113], v154 offset:23552
	buffer_load_dwordx4 v1, s[20:23], s69 offen lds
	s_mov_b32 m0, s38
	s_nop 0
	buffer_load_dwordx4 v252, s[20:23], s69 offen lds
	s_barrier
	s_waitcnt lgkmcnt(0)
	s_nop 0
	s_waitcnt lgkmcnt(6)
	v_mfma_f32_16x16x128_f8f6f4 v[62:65], v[126:133], v[66:73], 0
	v_mfma_f32_16x16x128_f8f6f4 v[58:61], v[138:145], v[66:73], 0
	s_waitcnt lgkmcnt(4)
	v_mfma_f32_16x16x128_f8f6f4 v[184:187], v[126:133], v[82:89], 0
	v_mfma_f32_16x16x128_f8f6f4 v[188:191], v[138:145], v[82:89], 0
	s_waitcnt lgkmcnt(2)
	v_mfma_f32_16x16x128_f8f6f4 v[216:219], v[126:133], v[98:105], 0
	v_mfma_f32_16x16x128_f8f6f4 v[220:223], v[138:145], v[98:105], 0
	s_waitcnt lgkmcnt(0)
	v_mfma_f32_16x16x128_f8f6f4 v[224:227], v[126:133], v[106:113], 0
	v_mfma_f32_16x16x128_f8f6f4 v[228:231], v[138:145], v[106:113], 0
	s_nop 0
	s_barrier
	s_add_i32 s70, s67, 0x40000
	s_mov_b32 m0, s39
	s_nop 0
	buffer_load_dwordx4 v253, s[24:27], s70 offen lds
	s_mov_b32 m0, s40
	s_nop 0
	buffer_load_dwordx4 v150, s[24:27], s70 offen lds
	s_waitcnt vmcnt(6)
	s_barrier
	s_nop 0
	v_mfma_f32_16x16x128_f8f6f4 v[54:57], v[74:81], v[66:73], 0
	v_mfma_f32_16x16x128_f8f6f4 v[50:53], v[90:97], v[66:73], 0
	v_mfma_f32_16x16x128_f8f6f4 v[232:235], v[74:81], v[82:89], 0
	v_mfma_f32_16x16x128_f8f6f4 v[236:239], v[90:97], v[82:89], 0
	v_mfma_f32_16x16x128_f8f6f4 v[240:243], v[74:81], v[98:105], 0
	v_mfma_f32_16x16x128_f8f6f4 v[244:247], v[90:97], v[98:105], 0
	v_mfma_f32_16x16x128_f8f6f4 v[248:251], v[74:81], v[106:113], 0
	v_mfma_f32_16x16x128_f8f6f4 v[146:149], v[90:97], v[106:113], 0
	s_nop 0
	s_barrier
	s_branch .Lmid_g2
.LBB0_1081:
	s_waitcnt lgkmcnt(0)
	ds_read_b128 v[126:129], v153
	ds_read_b128 v[130:133], v153 offset:1024
	ds_read_b128 v[138:141], v153 offset:2048
	ds_read_b128 v[142:145], v153 offset:3072
	s_add_i32 s26, s1, 0xfffc0080
	s_cmp_eq_u32 s66, 12
	s_cselect_b32 s69, s18, s26
	s_cselect_b32 s67, s0, s19
	s_or_b32 s68, s69, 0x80
	s_mov_b32 m0, s51
	ds_read_b128 v[160:163], v154
	ds_read_b128 v[164:167], v154 offset:1024
	ds_read_b128 v[168:171], v154 offset:2048
	ds_read_b128 v[172:175], v154 offset:3072
	ds_read_b128 v[176:179], v154 offset:4096
	ds_read_b128 v[180:183], v154 offset:5120
	ds_read_b128 v[184:187], v154 offset:6144
	ds_read_b128 v[188:191], v154 offset:7168
	buffer_load_dwordx4 v1, s[20:23], s1 offen lds
	s_mov_b32 m0, s52
	s_nop 0
	buffer_load_dwordx4 v252, s[20:23], s1 offen lds
	s_waitcnt lgkmcnt(8)
	s_barrier
	s_waitcnt lgkmcnt(0)
	s_nop 0
	s_waitcnt lgkmcnt(6)
	v_mfma_f32_16x16x128_f8f6f4 v[134:137], v[126:133], v[160:167], v[134:137]
	v_mfma_f32_16x16x128_f8f6f4 v[122:125], v[138:145], v[160:167], v[122:125]
	s_waitcnt lgkmcnt(4)
	v_mfma_f32_16x16x128_f8f6f4 v[192:195], v[126:133], v[168:175], v[110:113]
	v_mfma_f32_16x16x128_f8f6f4 v[196:199], v[138:145], v[168:175], v[106:109]
	s_waitcnt lgkmcnt(2)
	v_mfma_f32_16x16x128_f8f6f4 v[200:203], v[126:133], v[176:183], v[94:97]
	v_mfma_f32_16x16x128_f8f6f4 v[204:207], v[138:145], v[176:183], v[90:93]
	s_waitcnt lgkmcnt(0)
	v_mfma_f32_16x16x128_f8f6f4 v[208:211], v[126:133], v[184:191], v[78:81]
	v_mfma_f32_16x16x128_f8f6f4 v[212:215], v[138:145], v[184:191], v[74:77]
	s_nop 0
	s_barrier
	s_mov_b32 s26, s22
	s_mov_b32 s27, s23
	s_mov_b32 m0, s36
	s_nop 1
	ds_read_b128 v[74:77], v155
	ds_read_b128 v[78:81], v155 offset:1024
	ds_read_b128 v[90:93], v155 offset:2048
	ds_read_b128 v[94:97], v155 offset:3072
	buffer_load_dwordx4 v253, s[24:27], s67 offen lds
	s_mov_b32 m0, s37
	s_nop 0
	buffer_load_dwordx4 v150, s[24:27], s67 offen lds
	s_barrier
	s_waitcnt lgkmcnt(0)
	s_nop 0
	s_waitcnt lgkmcnt(2)
	v_mfma_f32_16x16x128_f8f6f4 v[118:121], v[74:81], v[160:167], v[118:121]
	s_waitcnt lgkmcnt(0)
	v_mfma_f32_16x16x128_f8f6f4 v[114:117], v[90:97], v[160:167], v[114:117]
	v_mfma_f32_16x16x128_f8f6f4 v[160:163], v[74:81], v[168:175], v[102:105]
	v_mfma_f32_16x16x128_f8f6f4 v[164:167], v[90:97], v[168:175], v[98:101]
	v_mfma_f32_16x16x128_f8f6f4 v[168:171], v[74:81], v[176:183], v[86:89]
	v_mfma_f32_16x16x128_f8f6f4 v[172:175], v[90:97], v[176:183], v[82:85]
	v_mfma_f32_16x16x128_f8f6f4 v[176:179], v[74:81], v[184:191], v[70:73]
	v_mfma_f32_16x16x128_f8f6f4 v[180:183], v[90:97], v[184:191], v[66:69]
	s_nop 0
	s_mov_b32 m0, s35
	s_barrier
	s_nop 3
	ds_read_b128 v[66:69], v154 offset:16384
	ds_read_b128 v[70:73], v154 offset:17408
	ds_read_b128 v[82:85], v154 offset:18432
	ds_read_b128 v[86:89], v154 offset:19456
	ds_read_b128 v[98:101], v154 offset:20480
	ds_read_b128 v[102:105], v154 offset:21504
	ds_read_b128 v[106:109], v154 offset:22528
	ds_read_b128 v[110:113], v154 offset:23552
	buffer_load_dwordx4 v1, s[20:23], s69 offen lds
	s_mov_b32 m0, s38
	s_nop 0
	buffer_load_dwordx4 v252, s[20:23], s69 offen lds
	s_barrier
	s_waitcnt lgkmcnt(0)
	s_nop 0
	s_waitcnt lgkmcnt(6)
	v_mfma_f32_16x16x128_f8f6f4 v[62:65], v[126:133], v[66:73], v[62:65]
	v_mfma_f32_16x16x128_f8f6f4 v[58:61], v[138:145], v[66:73], v[58:61]
	s_waitcnt lgkmcnt(4)
	v_mfma_f32_16x16x128_f8f6f4 v[184:187], v[126:133], v[82:89], v[46:49]
	v_mfma_f32_16x16x128_f8f6f4 v[188:191], v[138:145], v[82:89], v[42:45]
	s_waitcnt lgkmcnt(2)
	v_mfma_f32_16x16x128_f8f6f4 v[216:219], v[126:133], v[98:105], v[22:25]
	v_mfma_f32_16x16x128_f8f6f4 v[220:223], v[138:145], v[98:105], v[18:21]
	s_waitcnt lgkmcnt(0)
	v_mfma_f32_16x16x128_f8f6f4 v[224:227], v[126:133], v[106:113], v[6:9]
	v_mfma_f32_16x16x128_f8f6f4 v[228:231], v[138:145], v[106:113], v[2:5]
	s_nop 0
	s_barrier
	s_add_i32 s70, s67, 0x40000
	s_mov_b32 m0, s39
	s_nop 0
	buffer_load_dwordx4 v253, s[24:27], s70 offen lds
	s_mov_b32 m0, s40
	s_nop 0
	buffer_load_dwordx4 v150, s[24:27], s70 offen lds
	s_waitcnt vmcnt(6)
	s_barrier
	s_nop 0
	v_mfma_f32_16x16x128_f8f6f4 v[54:57], v[74:81], v[66:73], v[54:57]
	v_mfma_f32_16x16x128_f8f6f4 v[50:53], v[90:97], v[66:73], v[50:53]
	v_mfma_f32_16x16x128_f8f6f4 v[232:235], v[74:81], v[82:89], v[30:33]
	v_mfma_f32_16x16x128_f8f6f4 v[236:239], v[90:97], v[82:89], v[26:29]
	v_mfma_f32_16x16x128_f8f6f4 v[240:243], v[74:81], v[98:105], v[38:41]
	v_mfma_f32_16x16x128_f8f6f4 v[244:247], v[90:97], v[98:105], v[34:37]
	v_mfma_f32_16x16x128_f8f6f4 v[248:251], v[74:81], v[106:113], v[14:17]
	v_mfma_f32_16x16x128_f8f6f4 v[146:149], v[90:97], v[106:113], v[10:13]
	s_nop 0
	s_barrier
.Lmid_g2:
	ds_read_b128 v[2:5], v156
	ds_read_b128 v[6:9], v156 offset:1024
	s_nop 2
	ds_read_b128 v[10:13], v156 offset:2048
	ds_read_b128 v[14:17], v156 offset:3072
	s_add_i32 s69, s69, 0x40000
	s_mov_b32 m0, s41
	ds_read_b128 v[18:21], v154 offset:32768
	ds_read_b128 v[22:25], v154 offset:33792
	ds_read_b128 v[26:29], v154 offset:34816
	ds_read_b128 v[30:33], v154 offset:35840
	ds_read_b128 v[34:37], v154 offset:36864
	ds_read_b128 v[38:41], v154 offset:37888
	ds_read_b128 v[42:45], v154 offset:38912
	ds_read_b128 v[46:49], v154 offset:39936
	buffer_load_dwordx4 v1, s[20:23], s69 offen lds
	s_mov_b32 m0, s42
	s_nop 0
	buffer_load_dwordx4 v252, s[20:23], s69 offen lds
	s_waitcnt lgkmcnt(8)
	s_barrier
	s_waitcnt lgkmcnt(0)
	s_nop 0
	s_waitcnt lgkmcnt(6)
	v_mfma_f32_16x16x128_f8f6f4 v[134:137], v[2:9], v[18:25], v[134:137]
	v_mfma_f32_16x16x128_f8f6f4 v[122:125], v[10:17], v[18:25], v[122:125]
	s_waitcnt lgkmcnt(4)
	v_mfma_f32_16x16x128_f8f6f4 v[110:113], v[2:9], v[26:33], v[192:195]
	v_mfma_f32_16x16x128_f8f6f4 v[106:109], v[10:17], v[26:33], v[196:199]
	s_waitcnt lgkmcnt(2)
	v_mfma_f32_16x16x128_f8f6f4 v[94:97], v[2:9], v[34:41], v[200:203]
	v_mfma_f32_16x16x128_f8f6f4 v[90:93], v[10:17], v[34:41], v[204:207]
	s_waitcnt lgkmcnt(0)
	v_mfma_f32_16x16x128_f8f6f4 v[78:81], v[2:9], v[42:49], v[208:211]
	v_mfma_f32_16x16x128_f8f6f4 v[74:77], v[10:17], v[42:49], v[212:215]
	s_nop 0
	s_barrier
	s_add_i32 s69, s67, 0x80
	s_mov_b32 m0, s45
	ds_read_b128 v[126:129], v157
	ds_read_b128 v[130:133], v157 offset:1024
	ds_read_b128 v[138:141], v157 offset:2048
	ds_read_b128 v[142:145], v157 offset:3072
	buffer_load_dwordx4 v253, s[24:27], s69 offen lds
	s_mov_b32 m0, s46
	s_nop 0
	buffer_load_dwordx4 v150, s[24:27], s69 offen lds
	s_barrier
	s_waitcnt lgkmcnt(0)
	s_nop 0
	s_waitcnt lgkmcnt(2)
	v_mfma_f32_16x16x128_f8f6f4 v[118:121], v[126:133], v[18:25], v[118:121]
	s_waitcnt lgkmcnt(0)
	v_mfma_f32_16x16x128_f8f6f4 v[114:117], v[138:145], v[18:25], v[114:117]
	v_mfma_f32_16x16x128_f8f6f4 v[102:105], v[126:133], v[26:33], v[160:163]
	v_mfma_f32_16x16x128_f8f6f4 v[98:101], v[138:145], v[26:33], v[164:167]
	v_mfma_f32_16x16x128_f8f6f4 v[86:89], v[126:133], v[34:41], v[168:171]
	v_mfma_f32_16x16x128_f8f6f4 v[82:85], v[138:145], v[34:41], v[172:175]
	v_mfma_f32_16x16x128_f8f6f4 v[70:73], v[126:133], v[42:49], v[176:179]
	v_mfma_f32_16x16x128_f8f6f4 v[66:69], v[138:145], v[42:49], v[180:183]
	s_nop 0
	s_mov_b32 m0, s47
	s_barrier
	ds_read_b128 v[26:29], v154 offset:49152
	ds_read_b128 v[30:33], v154 offset:50176
	ds_read_b128 v[34:37], v154 offset:51200
	ds_read_b128 v[38:41], v154 offset:52224
	ds_read_b128 v[160:163], v154 offset:53248
	ds_read_b128 v[164:167], v154 offset:54272
	ds_read_b128 v[168:171], v154 offset:55296
	ds_read_b128 v[172:175], v154 offset:56320
	buffer_load_dwordx4 v1, s[20:23], s68 offen lds
	s_mov_b32 m0, s48
	s_nop 0
	buffer_load_dwordx4 v252, s[20:23], s68 offen lds
	s_barrier
	s_waitcnt lgkmcnt(0)
	s_nop 0
	s_waitcnt lgkmcnt(6)
	v_mfma_f32_16x16x128_f8f6f4 v[62:65], v[2:9], v[26:33], v[62:65]
	v_mfma_f32_16x16x128_f8f6f4 v[58:61], v[10:17], v[26:33], v[58:61]
	s_waitcnt lgkmcnt(4)
	v_mfma_f32_16x16x128_f8f6f4 v[46:49], v[2:9], v[34:41], v[184:187]
	v_mfma_f32_16x16x128_f8f6f4 v[42:45], v[10:17], v[34:41], v[188:191]
	s_waitcnt lgkmcnt(2)
	v_mfma_f32_16x16x128_f8f6f4 v[22:25], v[2:9], v[160:167], v[216:219]
	v_mfma_f32_16x16x128_f8f6f4 v[18:21], v[10:17], v[160:167], v[220:223]
	s_waitcnt lgkmcnt(0)
	v_mfma_f32_16x16x128_f8f6f4 v[6:9], v[2:9], v[168:175], v[224:227]
	v_mfma_f32_16x16x128_f8f6f4 v[2:5], v[10:17], v[168:175], v[228:231]
	s_nop 0
	s_barrier
	s_add_i32 s67, s67, 0x40080
	s_mov_b32 m0, s49
	s_nop 0
	buffer_load_dwordx4 v253, s[24:27], s67 offen lds
	s_mov_b32 m0, s50
	s_nop 0
	buffer_load_dwordx4 v150, s[24:27], s67 offen lds
	s_waitcnt vmcnt(6)
	s_barrier
; #define LAS __attribute__((address_space(3)))
;     __device__ __forceinline__ void operator()(const f32x4 (&acc)[2][2][4][2], const Unit& u, int wr, int wc, int fr, int fq, LAS const unsigned char* tbl, LAS const unsigned char* b2l) const {
;         { int t_ = threadIdx.x; asm volatile("" : "+v"(t_)); fr = t_ & 15; fq = (t_ >> 4) & 3; }
;         const int r0 = wr * 64 + fr; const int col0 = u.pn * BM + wc * 32 + 8 * fq;
;         unsigned char* Y = ws + WS_Y;
;         f32x4 bv[2][2];
; #pragma unroll
;         for (int bj = 0; bj < 2; ++bj)
; #pragma unroll
;             for (int n = 0; n < 2; ++n) bv[bj][n] = *(LAS const f32x4*)(b2l + (wc * 32 + 8 * fq + bj * HALF + 4 * n) * 4);
; #pragma unroll
;         for (int ai = 0; ai < 2; ++ai)
; #pragma unroll
;             for (int m = 0; m < 4; ++m) { const int row = r0 + ai * HALF + m * 16;
;                 if (u.pos0 + row < u.cnt) { const int pid = *(LAS const int*)(tbl + row * 4); const float gt = *(LAS const float*)(tbl + 1024 + row * 4) * Y_FP8_SCALE; unsigned char* rowp = Y + (size_t)pid * D_ + col0;
; #pragma unroll
;                     for (int bj = 0; bj < 2; ++bj) { const f32x4 v0 = (acc[ai][bj][m][0] * (1.0f / W_FP8_SCALE) + bv[bj][0]) * gt, v1 = (acc[ai][bj][m][1] * (1.0f / W_FP8_SCALE) + bv[bj][1]) * gt;
;                         u32x2 w; w.x = pk4_fp8(v0[0], v0[1], v0[2], v0[3]); w.y = pk4_fp8(v1[0], v1[1], v1[2], v1[3]);
;                         *(u32x2*)(rowp + bj * HALF) = w; } } }
	s_nop 0
	v_mfma_f32_16x16x128_f8f6f4 v[54:57], v[126:133], v[26:33], v[54:57]
	v_mfma_f32_16x16x128_f8f6f4 v[50:53], v[138:145], v[26:33], v[50:53]
	v_mfma_f32_16x16x128_f8f6f4 v[30:33], v[126:133], v[34:41], v[232:235]
	v_mfma_f32_16x16x128_f8f6f4 v[26:29], v[138:145], v[34:41], v[236:239]
	v_mfma_f32_16x16x128_f8f6f4 v[38:41], v[126:133], v[160:167], v[240:243]
	v_mfma_f32_16x16x128_f8f6f4 v[34:37], v[138:145], v[160:167], v[244:247]
	v_mfma_f32_16x16x128_f8f6f4 v[14:17], v[126:133], v[168:175], v[248:251]
	v_mfma_f32_16x16x128_f8f6f4 v[10:13], v[138:145], v[168:175], v[146:149]
	s_nop 0
	s_add_i32 s66, s66, 2
	s_addk_i32 s1, 0x100
	s_addk_i32 s19, 0x100
	s_cmp_gt_u32 s66, 13
	s_barrier
	s_cbranch_scc0 .LBB0_1081
	s_lshl_b32 s0, s65, 11
	s_add_i32 s18, s0, 0
	s_lshl_b32 s0, s65, 10
	s_add_i32 s18, s18, 0x20000
	s_add_i32 s0, s0, 0x21800
	v_mov_b32_e32 v146, v0
	s_cmp_lt_i32 s65, 2
	s_cselect_b32 s0, s0, 0x23800
	v_lshrrev_b32_e32 v126, 1, v146
	v_and_b32_e32 v147, 24, v126
	s_add_i32 s0, s0, 0
	v_or_b32_e32 v126, s44, v147
	v_lshl_add_u32 v126, v126, 2, s0
	ds_read_b128 v[142:145], v126
	ds_read_b128 v[138:141], v126 offset:16
	ds_read_b128 v[130:133], v126 offset:512
	ds_read_b128 v[126:129], v126 offset:528
	s_lshl_b32 s0, s64, 8
	s_or_b32 s0, s0, s44
	v_and_or_b32 v159, v146, 15, s43
	v_or_b32_e32 v146, s0, v147
	v_ashrrev_i32_e32 v147, 31, v146
	v_add_u32_e32 v148, s34, v159
	v_lshl_add_u64 v[146:147], s[6:7], 0, v[146:147]
	v_cmp_gt_i32_e32 vcc, s33, v148
	s_and_saveexec_b64 s[0:1], vcc
	s_cbranch_execz .LBB0_1084
	v_lshl_add_u32 v148, v159, 2, s18
	ds_read2st64_b32 v[148:149], v148 offset1:4
	s_waitcnt lgkmcnt(4)
	v_pk_fma_f32 v[134:135], v[134:135], s[28:29], v[142:143] op_sel_hi:[1,0,1]
	v_pk_fma_f32 v[136:137], v[136:137], s[28:29], v[144:145] op_sel_hi:[1,0,1]
	s_waitcnt lgkmcnt(3)
	v_pk_fma_f32 v[124:125], v[124:125], s[28:29], v[140:141] op_sel_hi:[1,0,1]
	v_pk_fma_f32 v[122:123], v[122:123], s[28:29], v[138:139] op_sel_hi:[1,0,1]
	s_waitcnt lgkmcnt(0)
	v_ashrrev_i32_e32 v161, 31, v148
	v_mov_b32_e32 v160, v148
	v_mul_f32_e32 v148, 0x41800000, v149
	v_pk_mul_f32 v[134:135], v[134:135], v[148:149] op_sel_hi:[1,0]
	v_pk_mul_f32 v[136:137], v[136:137], v[148:149] op_sel_hi:[1,0]
	v_pk_mul_f32 v[124:125], v[124:125], v[148:149] op_sel_hi:[1,0]
	v_pk_mul_f32 v[122:123], v[122:123], v[148:149] op_sel_hi:[1,0]
	v_med3_f32 v149, v134, s55, v158
	v_med3_f32 v135, v135, s55, v158
	v_cvt_pk_fp8_f32 v134, v149, v135
	v_med3_f32 v122, v122, s55, v158
	v_med3_f32 v123, v123, s55, v158
	v_cvt_pk_fp8_f32 v135, v122, v123
	v_pk_fma_f32 v[118:119], v[118:119], s[28:29], v[130:131] op_sel_hi:[1,0,1]
	v_med3_f32 v122, v124, s55, v158
	v_med3_f32 v123, v125, s55, v158
	v_pk_mul_f32 v[118:119], v[118:119], v[148:149] op_sel_hi:[1,0]
	v_pk_fma_f32 v[114:115], v[114:115], s[28:29], v[126:127] op_sel_hi:[1,0,1]
	v_cvt_pk_fp8_f32 v135, v122, v123 op_sel:[0,0,1]
	v_pk_mul_f32 v[114:115], v[114:115], v[148:149] op_sel_hi:[1,0]
	v_med3_f32 v122, v118, s55, v158
	v_med3_f32 v119, v119, s55, v158
	v_cvt_pk_fp8_f32 v118, v122, v119
	v_med3_f32 v114, v114, s55, v158
	v_med3_f32 v115, v115, s55, v158
	v_cvt_pk_fp8_f32 v119, v114, v115
	v_pk_fma_f32 v[120:121], v[120:121], s[28:29], v[132:133] op_sel_hi:[1,0,1]
	v_pk_fma_f32 v[116:117], v[116:117], s[28:29], v[128:129] op_sel_hi:[1,0,1]
	v_med3_f32 v136, v136, s55, v158
	v_med3_f32 v137, v137, s55, v158
	v_pk_mul_f32 v[120:121], v[120:121], v[148:149] op_sel_hi:[1,0]
	v_pk_mul_f32 v[116:117], v[116:117], v[148:149] op_sel_hi:[1,0]
	v_cvt_pk_fp8_f32 v134, v136, v137 op_sel:[0,0,1]
	v_med3_f32 v120, v120, s55, v158
	v_med3_f32 v121, v121, s55, v158
	v_med3_f32 v114, v116, s55, v158
	v_med3_f32 v115, v117, s55, v158
	v_cvt_pk_fp8_f32 v118, v120, v121 op_sel:[0,0,1]
	v_cvt_pk_fp8_f32 v119, v114, v115 op_sel:[0,0,1]
	v_lshlrev_b64 v[114:115], 11, v[160:161]
	v_lshl_add_u64 v[114:115], v[146:147], 0, v[114:115]
	global_store_dwordx2 v[114:115], v[134:135], off
	global_store_dwordx2 v[114:115], v[118:119], off offset:128
